# gMLP / retention-KV work queue: next ticket requested one unit ahead (no atomic round trip at unit start)
# baseline (speedup 1.0000x reference)
; #define LAS __attribute__((address_space(3)))
; __global__ void __launch_bounds__(512, 2) mk_fwd(Args a) {
;     ...
;         for (int i = tid; i < 4096; i += 512) ((LAS float*)(lds + RP_ROT))[i] = rotc[i];
;         unsigned* qctr3 = (unsigned*)(ws + WS_CTL) + 8192 + 256;
;         for (;;) {
;             __syncthreads();
;             if (tid == 0) *(volatile LAS unsigned*)(lds + LDS_BARW + 32) = atomicAdd(qctr3, 1u);
;             __syncthreads();
;             const unsigned u = *(volatile LAS unsigned*)(lds + LDS_BARW + 32);
;             if (u >= 136u + (unsigned)(NB * 8 * NRC)) break;
;             if (u < 136u) gmlp_fast_unit((int)u, Pb, a.in[I_GMLPN], (const bf16_t*)(ws + WS_GMW), a.in[I_GMLPB], AO, lds);
;             else retp_kv_unit((int)u - 136, Pb, rotc, a.in[I_GAMMA], (bf16_t*)(ws + WS_OF), lds);
.LBB0_273:
	s_or_b64 exec, exec, s[0:1]
	v_or_b32_e32 v3, 0x200, v0
	v_bfe_u32 v4, v0, 2, 1
	v_lshlrev_b32_e32 v2, 3, v0
	v_lshrrev_b32_e32 v153, 4, v3
	v_or_b32_e32 v5, 0x600, v0
	v_lshlrev_b32_e32 v124, 6, v4
	v_and_b32_e32 v126, 24, v2
	v_lshrrev_b32_e32 v139, 3, v3
	v_lshrrev_b32_e32 v147, 4, v0
	v_xor_b32_e32 v3, 0x7f, v153
	s_add_u32 s16, s94, 0x8400
	v_or_b32_e32 v6, v124, v126
	v_bfe_u32 v10, v0, 4, 2
	v_cvt_f32_ubyte0_e32 v154, v3
	v_xor_b32_e32 v3, 63, v147
	v_lshrrev_b32_e32 v160, 4, v5
	s_addc_u32 s17, s95, 0
	v_lshl_add_u32 v8, v6, 1, 0
	v_bfe_u32 v6, v0, 2, 2
	s_add_i32 s3, 0, 0x12000
	v_cvt_f32_ubyte0_e32 v158, v3
	v_xor_b32_e32 v3, 0x7f, v160
	v_lshlrev_b32_e32 v128, 3, v10
	s_movk_i32 s2, 0x120
	v_cvt_f32_ubyte0_e32 v161, v3
	v_or_b32_e32 v3, v128, v6
	v_mov_b32_e32 v6, s3
	v_mad_u32_u24 v13, v3, s2, v6
	v_mov_b32_e32 v6, 0x2400
	v_mad_u32_u24 v165, v3, s2, v6
	v_mov_b32_e32 v6, 0x4800
	v_and_b32_e32 v146, 15, v0
	v_mad_u32_u24 v167, v3, s2, v6
	v_mov_b32_e32 v6, 0x6c00
	v_lshlrev_b32_e32 v12, 4, v146
	v_mad_u32_u24 v168, v3, s2, v6
	v_add_u32_e32 v149, s3, v12
	v_add_u32_e32 v14, s3, v165
	v_add_u32_e32 v166, s3, v126
	v_add_u32_e32 v15, s3, v167
	v_add_u32_e32 v16, s3, v168
	v_readlane_b32 s2, v254, 63
	v_xor_b32_e32 v7, 0x7f, v147
	v_lshlrev_b32_e32 v122, 8, v146
	v_readlane_b32 s3, v255, 0
	v_cvt_f32_ubyte0_e32 v150, v7
	v_mul_u32_u24_e32 v5, 0x120, v3
	v_lshl_add_u64 v[6:7], s[2:3], 0, v[122:123]
	v_mov_b32_e32 v129, v123
	v_mov_b32_e32 v3, v123
	v_lshl_add_u64 v[130:131], v[6:7], 0, v[128:129]
	v_lshl_add_u64 v[132:133], s[62:63], 0, v[2:3]
	v_add_u32_e32 v129, 0, v2
	v_lshl_add_u64 v[134:135], s[66:67], 0, v[2:3]
	v_and_b32_e32 v2, 3, v0
	v_and_b32_e32 v3, 0x1fc, v0
	v_lshlrev_b32_e32 v122, 9, v2
	v_cmp_eq_u32_e64 s[6:7], 0, v2
	v_add_u32_e32 v177, 0, v3
	v_lshl_add_u64 v[2:3], s[94:95], 0, v[122:123]
	s_mov_b64 s[2:3], 0x41e01820
	v_lshl_add_u64 v[136:137], v[2:3], 0, s[2:3]
	v_lshl_add_u32 v2, v146, 2, 0
	v_lshrrev_b32_e32 v127, 3, v0
	v_add_u32_e32 v183, 0xb000, v2
	v_cmp_eq_u32_e64 s[4:5], 0, v4
	v_mul_u32_u24_e32 v9, 0x120, v127
	v_mul_u32_u24_e32 v11, 0x120, v139
	v_lshlrev_b32_e32 v4, 3, v146
	v_or_b32_e32 v157, 64, v147
	v_add3_u32 v164, 0, v5, v126
	v_lshl_add_u32 v6, v146, 5, 0
	v_mbcnt_lo_u32_b32 v2, -1, 0
	v_cmp_eq_u32_e64 s[0:1], 0, v0
	v_lshrrev_b32_e32 v1, 2, v0
	v_lshlrev_b32_e32 v125, 2, v126
	v_add_u32_e32 v148, 0, v12
	v_cvt_f32_ubyte0_e32 v151, v147
	v_mul_u32_u24_e32 v152, 0x120, v147
	v_cvt_f32_ubyte0_e32 v155, v153
	v_mul_u32_u24_e32 v156, 0x120, v153
	v_cvt_f32_ubyte0_e32 v159, v157
	v_cvt_f32_ubyte0_e32 v162, v160
	v_mul_u32_u24_e32 v163, 0x120, v160
	v_add_u32_e32 v169, 0xfc00, v164
	v_add_u32_e32 v170, 0xfc20, v164
	v_add_u32_e32 v171, 0xfc40, v164
	v_add_u32_e32 v172, 0xfc60, v164
	v_add_u32_e32 v173, 0xfc80, v164
	v_add_u32_e32 v174, 0xfca0, v164
	v_add_u32_e32 v175, 0xfcc0, v164
	v_add_u32_e32 v176, 0xfce0, v164
	v_sub_u32_e32 v178, v6, v12
	v_lshl_add_u32 v179, v147, 2, 0
	v_lshl_add_u32 v180, v153, 2, 0
	v_lshl_add_u32 v181, v160, 2, 0
	v_add3_u32 v182, 0, v126, v5
	v_lshlrev_b32_e32 v138, 4, v10
	v_add_u32_e32 v184, 0xa000, v6
	v_or_b32_e32 v140, 0x41e01800, v12
	v_mov_b32_e32 v141, v123
	s_add_i32 s25, 0, 0x23fe0
	s_movk_i32 s26, 0x4000
	s_movk_i32 s27, 0x3000
	s_mov_b64 s[18:19], 0x2000
	v_add_u32_e32 v185, v8, v9
	s_movk_i32 s34, 0x100
	s_mov_b32 s35, 0xbfb8aa3b
	s_mov_b32 s36, 0x42ce8ed0
	s_mov_b32 s37, 0xc2b17218
	s_mov_b32 s38, 0x7f800000
	s_mov_b32 s39, 0x33800000
	s_mov_b32 s40, 0x3f2aaaab
	v_mov_b32_e32 v186, 0x3ecc95a3
	s_mov_b32 s41, 0x3f317218
	v_add_u32_e32 v187, v8, v11
	v_lshlrev_b32_e32 v142, 1, v4
	s_mov_b32 s42, 0xc2fc0000
	s_movk_i32 s43, 0x6000
	v_mov_b32_e32 v188, 0x358637bd
	s_mov_b64 s[20:21], 0x100
	v_mov_b32_e32 v189, 0x7f800000
	v_mov_b32_e32 v144, 0x3f317218
	v_mov_b32_e32 v190, 0x42800000
	v_not_b32_e32 v191, 63
	v_add_u32_e32 v192, v13, v126
	v_add_u32_e32 v193, v14, v126
	v_add_u32_e32 v194, v15, v126
	v_add_u32_e32 v195, v16, v126
	v_mbcnt_hi_u32_b32 v196, -1, v2
	s_and_saveexec_b64 s[2:3], s[0:1]
	v_mov_b32_e32 v3, 1
	global_atomic_add v251, v123, v3, s[16:17] sc0
	s_waitcnt vmcnt(0)
	s_mov_b64 exec, s[2:3]
	s_branch .LBB0_276

; #define LAS __attribute__((address_space(3)))
; __global__ void __launch_bounds__(512, 2) mk_fwd(Args a) {
;     ...
;         for (;;) {
;             __syncthreads();
;             if (tid == 0) *(volatile LAS unsigned*)(lds + LDS_BARW + 32) = atomicAdd(qctr3, 1u);
;             __syncthreads();
;             const unsigned u = *(volatile LAS unsigned*)(lds + LDS_BARW + 32);
.LBB0_276:
	s_waitcnt lgkmcnt(0)
	s_barrier
	s_and_saveexec_b64 s[2:3], s[0:1]
	s_cbranch_execz .LBB0_280
	v_mov_b32_e32 v3, s25
	ds_write_b32 v3, v251
	v_mov_b32_e32 v2, 1
	s_nop 0
	global_atomic_add v251, v123, v2, s[16:17] sc0
